# speedup vs baseline: 1.0005x; 1.0005x over previous
.Lka_done:
	v_mfma_f32_32x32x16_bf16 a[16:31], v[176:179], v[144:147], a[16:31]
	v_cvt_pk_bf16_f32 v228, v227, v228
	v_cvt_pk_bf16_f32 v229, v229, v230
	v_cvt_pk_bf16_f32 v230, v231, v232
	v_cvt_pk_bf16_f32 v231, v233, v234
	v_max3_f32 v156, v112, v113, v80
	v_max3_f32 v157, v114, v115, v81
	v_mfma_f32_32x32x16_bf16 a[32:47], v[168:171], v[128:131], a[32:47]
	v_max3_f32 v156, v156, v82, v83
	ds_read_b128 a[224:227], v217 offset:8192
	v_max3_f32 v156, v156, v116, v117
	v_max3_f32 v157, v157, v118, v119
	v_max3_f32 v156, v156, v84, v85
	v_max3_f32 v157, v157, v86, v87
	v_mfma_f32_32x32x16_bf16 a[48:63], v[168:171], v[144:147], a[48:63]
	ds_read_b128 a[228:231], v199 offset:8192
	v_max3_f32 v156, v156, v120, v121
	v_max3_f32 v157, v157, v122, v123
	v_max3_f32 v156, v156, v88, v89
	v_max3_f32 v157, v157, v90, v91
	ds_read_b128 a[232:235], v198 offset:8192
	v_mfma_f32_32x32x16_bf16 a[64:79], v[160:163], v[128:131], a[64:79]
	v_max3_f32 v156, v156, v124, v125
	v_max3_f32 v157, v157, v126, v127
	v_max3_f32 v156, v156, v92, v93
	v_max3_f32 v157, v157, v94, v95
	ds_read_b128 a[236:239], v197 offset:8192
	v_max3_f32 v158, v96, v97, v64
	v_mfma_f32_32x32x16_bf16 a[80:95], v[160:163], v[144:147], a[80:95]
	v_max3_f32 v159, v98, v99, v65
	v_max3_f32 v158, v158, v66, v67
	v_cvt_pk_bf16_f32 v160, v148, v149
	v_cvt_pk_bf16_f32 v161, v150, v151
	v_cvt_pk_bf16_f32 v162, v152, v153
	v_cvt_pk_bf16_f32 v163, v154, v155
	v_mfma_f32_32x32x16_bf16 a[96:111], v[136:139], v[128:131], a[96:111]
	ds_read_b128 a[240:243], v217 offset:8320
	v_max3_f32 v158, v158, v100, v101
	v_max3_f32 v159, v159, v102, v103
	v_max3_f32 v158, v158, v68, v69
	v_max3_f32 v159, v159, v70, v71
	ds_read_b128 a[244:247], v199 offset:8320
	v_mfma_f32_32x32x16_bf16 a[112:127], v[136:139], v[144:147], a[112:127]
	v_max3_f32 v128, v158, v104, v105
	v_max3_f32 v129, v159, v106, v107
	v_max3_f32 v128, v128, v72, v73
	v_max3_f32 v129, v129, v74, v75
	ds_read_b128 a[248:251], v198 offset:8320
	v_max3_f32 v128, v128, v108, v109
	v_mfma_f32_32x32x16_bf16 a[0:15], v[132:135], v[52:55], a[0:15]
	v_max3_f32 v129, v129, v110, v111
	v_max3_f32 v128, v128, v76, v77
	v_max3_f32 v130, v129, v78, v79
	ds_read_b128 a[252:255], v197 offset:8320
	s_cmp_gt_u32 s27, 4
	s_cbranch_scc1 .Lkb2_done
	s_waitcnt lgkmcnt(8)
	v_pk_add_f32 v[200:201], v[248:249], v[200:201]
	v_pk_add_f32 v[202:203], v[250:251], v[202:203]
	v_pk_add_f32 v[204:205], v[252:253], v[204:205]
	v_pk_add_f32 v[206:207], v[254:255], v[206:207]
	v_cvt_pk_bf16_f32 v248, v248, v249
	v_cvt_pk_bf16_f32 v249, v250, v251
	v_cvt_pk_bf16_f32 v250, v252, v253
	v_cvt_pk_bf16_f32 v251, v254, v255
	v_lshrrev_b32_e32 v252, 1, v208
	buffer_store_dwordx4 v[248:251], v252, s[4:7], s56 offen sc1
	s_add_i32 s56, s56, 0x1000
	s_nop 1
	global_load_dwordx4 v[248:251], v208, s[54:55] nt
	global_load_dwordx4 v[252:255], v208, s[54:55] offset:16 nt
	s_add_u32 s54, s54, 0x2000
	s_addc_u32 s55, s55, 0
	s_mov_b32 m0, s84
	s_nop 0
	buffer_load_dwordx4 v208, s[80:83], s86 offen lds
	s_mov_b32 m0, s85
	s_nop 0
	buffer_load_dwordx4 v208, s[80:83], s86 offen offset:16 lds
	s_add_i32 s86, s86, 0x2000

.LBB0_18:
	v_mfma_f32_32x32x16_bf16 a[48:63], v[60:63], v[140:143], a[48:63]
	v_exp_f32_e32 v128, v112
	v_exp_f32_e32 v129, v113
	v_exp_f32_e32 v130, v114
	v_exp_f32_e32 v131, v115
	v_mfma_f32_32x32x16_bf16 a[64:79], v[56:59], v[52:55], a[64:79]
	v_exp_f32_e32 v132, v116
	v_exp_f32_e32 v133, v117
	v_exp_f32_e32 v134, v118
	v_exp_f32_e32 v135, v119
	v_mfma_f32_32x32x16_bf16 a[80:95], v[56:59], v[140:143], a[80:95]
	v_add_f32_e32 v56, v128, v130
	v_add_f32_e32 v57, v129, v131
	v_exp_f32_e32 v136, v120
	v_exp_f32_e32 v137, v121
	v_exp_f32_e32 v138, v122
	v_mfma_f32_32x32x16_bf16 a[96:111], v[48:51], v[52:55], a[96:111]
	v_add_f32_e32 v52, v56, v132
	v_add_f32_e32 v53, v57, v133
	v_add_f32_e32 v52, v52, v134
	v_exp_f32_e32 v139, v123
	v_exp_f32_e32 v144, v96
	v_mfma_f32_32x32x16_bf16 a[112:127], v[48:51], v[140:143], a[112:127]
	v_add_f32_e32 v48, v53, v135
	v_add_f32_e32 v49, v52, v136
	v_exp_f32_e32 v140, v124
	v_exp_f32_e32 v141, v125
	v_add_f32_e32 v48, v48, v137
	v_mfma_f32_32x32x16_bf16 a[0:15], v[44:47], v[228:231], a[0:15]
	v_add_f32_e32 v49, v49, v138
	v_add_f32_e32 v48, v48, v139
	v_exp_f32_e32 v142, v126
	v_exp_f32_e32 v143, v127
	v_exp_f32_e32 v145, v97
	v_mfma_f32_32x32x16_bf16 a[16:31], v[44:47], v[160:163], a[16:31]
	v_add_f32_e32 v44, v49, v140
	v_add_f32_e32 v45, v48, v141
	v_exp_f32_e32 v146, v98
	v_add_f32_e32 v236, v44, v142
	v_add_f32_e32 v235, v45, v143
	v_exp_f32_e32 v147, v99
	v_mfma_f32_32x32x16_bf16 a[32:47], v[40:43], v[228:231], a[32:47]
	v_exp_f32_e32 v148, v100
	v_exp_f32_e32 v149, v101
	v_exp_f32_e32 v150, v102
	v_exp_f32_e32 v151, v103
	v_mfma_f32_32x32x16_bf16 a[48:63], v[40:43], v[160:163], a[48:63]
	v_add_f32_e32 v41, v144, v146
	v_add_f32_e32 v40, v145, v147
	v_add_f32_e32 v41, v41, v148
	v_add_f32_e32 v40, v40, v149
	v_exp_f32_e32 v152, v104
	v_exp_f32_e32 v153, v105
	v_mfma_f32_32x32x16_bf16 a[64:79], v[36:39], v[228:231], a[64:79]
	v_exp_f32_e32 v154, v106
	v_exp_f32_e32 v155, v107
	v_exp_f32_e32 v156, v108
	v_exp_f32_e32 v157, v109
	v_mfma_f32_32x32x16_bf16 a[80:95], v[36:39], v[160:163], a[80:95]
	v_add_f32_e32 v36, v41, v150
	v_add_f32_e32 v37, v40, v151
	v_add_f32_e32 v36, v36, v152
	v_add_f32_e32 v37, v37, v153
	v_add_f32_e32 v36, v36, v154
	v_exp_f32_e32 v158, v110
	v_mfma_f32_32x32x16_bf16 a[96:111], v[32:35], v[228:231], a[96:111]
	v_exp_f32_e32 v159, v111
	v_mfma_f32_32x32x16_bf16 a[112:127], v[32:35], v[160:163], a[112:127]
	v_add_f32_e32 v32, v37, v155
	v_add_f32_e32 v33, v36, v156
	s_andn2_b64 vcc, exec, s[0:1]
	v_add_f32_e32 v32, v32, v157
	v_add_f32_e32 v237, v33, v158
	s_nop 0
	v_add_f32_e32 v238, v32, v159
	s_cbranch_vccz .LBB0_23

.Lkc_done:
	v_mfma_f32_32x32x16_bf16 a[16:31], v[172:175], v[144:147], a[16:31]
	v_cvt_pk_bf16_f32 v228, v227, v228
	v_cvt_pk_bf16_f32 v229, v229, v230
	v_cvt_pk_bf16_f32 v230, v231, v232
	v_cvt_pk_bf16_f32 v231, v233, v234
	v_max3_f32 v156, v112, v113, v48
	v_max3_f32 v157, v114, v115, v49
	v_mfma_f32_32x32x16_bf16 a[32:47], v[164:167], v[128:131], a[32:47]
	v_max3_f32 v156, v156, v50, v51
	ds_read_b128 a[224:227], v218 offset:8192
	v_max3_f32 v156, v156, v116, v117
	v_max3_f32 v157, v157, v118, v119
	v_max3_f32 v156, v156, v52, v53
	v_max3_f32 v157, v157, v54, v55
	v_mfma_f32_32x32x16_bf16 a[48:63], v[164:167], v[144:147], a[48:63]
	ds_read_b128 a[228:231], v219 offset:8192
	v_max3_f32 v156, v156, v120, v121
	v_max3_f32 v157, v157, v122, v123
	v_max3_f32 v156, v156, v56, v57
	v_max3_f32 v157, v157, v58, v59
	ds_read_b128 a[232:235], v220 offset:8192
	v_mfma_f32_32x32x16_bf16 a[64:79], v[160:163], v[128:131], a[64:79]
	v_max3_f32 v156, v156, v124, v125
	v_max3_f32 v157, v157, v126, v127
	v_max3_f32 v156, v156, v60, v61
	v_max3_f32 v157, v157, v62, v63
	ds_read_b128 a[236:239], v221 offset:8192
	v_max3_f32 v158, v96, v97, v32
	v_mfma_f32_32x32x16_bf16 a[80:95], v[160:163], v[144:147], a[80:95]
	v_max3_f32 v159, v98, v99, v33
	v_max3_f32 v158, v158, v34, v35
	v_cvt_pk_bf16_f32 v160, v148, v149
	v_cvt_pk_bf16_f32 v161, v150, v151
	v_cvt_pk_bf16_f32 v162, v152, v153
	v_cvt_pk_bf16_f32 v163, v154, v155
	v_mfma_f32_32x32x16_bf16 a[96:111], v[136:139], v[128:131], a[96:111]
	ds_read_b128 a[240:243], v218 offset:8320
	v_max3_f32 v158, v158, v100, v101
	v_max3_f32 v159, v159, v102, v103
	v_max3_f32 v158, v158, v36, v37
	v_max3_f32 v159, v159, v38, v39
	ds_read_b128 a[244:247], v219 offset:8320
	v_mfma_f32_32x32x16_bf16 a[112:127], v[136:139], v[144:147], a[112:127]
	v_max3_f32 v128, v158, v104, v105
	v_max3_f32 v129, v159, v106, v107
	v_max3_f32 v128, v128, v40, v41
	v_max3_f32 v129, v129, v42, v43
	ds_read_b128 a[248:251], v220 offset:8320
	v_max3_f32 v128, v128, v108, v109
	v_mfma_f32_32x32x16_bf16 a[0:15], v[132:135], v[84:87], a[0:15]
	v_max3_f32 v129, v129, v110, v111
	v_max3_f32 v128, v128, v44, v45
	v_max3_f32 v130, v129, v46, v47
	ds_read_b128 a[252:255], v221 offset:8320
	s_cmp_gt_u32 s27, 4
	s_cbranch_scc1 .Lkd2_done
	s_waitcnt lgkmcnt(8)
	v_pk_add_f32 v[200:201], v[248:249], v[200:201]
	v_pk_add_f32 v[202:203], v[250:251], v[202:203]
	v_pk_add_f32 v[204:205], v[252:253], v[204:205]
	v_pk_add_f32 v[206:207], v[254:255], v[206:207]
	v_cvt_pk_bf16_f32 v248, v248, v249
	v_cvt_pk_bf16_f32 v249, v250, v251
	v_cvt_pk_bf16_f32 v250, v252, v253
	v_cvt_pk_bf16_f32 v251, v254, v255
	v_lshrrev_b32_e32 v252, 1, v208
	buffer_store_dwordx4 v[248:251], v252, s[4:7], s56 offen sc1
	s_add_i32 s56, s56, 0x1000
	s_nop 1
	global_load_dwordx4 v[248:251], v208, s[54:55] nt
	global_load_dwordx4 v[252:255], v208, s[54:55] offset:16 nt
	s_add_u32 s54, s54, 0x2000
	s_addc_u32 s55, s55, 0
	s_cmp_gt_u32 s27, 2
	s_cbranch_scc1 .Lkd2_done
	s_mov_b32 m0, s84
	s_nop 0
	buffer_load_dwordx4 v208, s[80:83], s86 offen lds
	s_mov_b32 m0, s85
	s_nop 0
	buffer_load_dwordx4 v208, s[80:83], s86 offen offset:16 lds
	s_add_i32 s86, s86, 0x2000

.LBB0_20:
	v_mfma_f32_32x32x16_bf16 a[48:63], v[92:95], v[140:143], a[48:63]
	v_exp_f32_e32 v128, v112
	v_exp_f32_e32 v129, v113
	v_exp_f32_e32 v130, v114
	v_exp_f32_e32 v131, v115
	v_mfma_f32_32x32x16_bf16 a[64:79], v[88:91], v[84:87], a[64:79]
	v_exp_f32_e32 v132, v116
	v_exp_f32_e32 v133, v117
	v_exp_f32_e32 v134, v118
	v_exp_f32_e32 v135, v119
	v_mfma_f32_32x32x16_bf16 a[80:95], v[88:91], v[140:143], a[80:95]
	v_add_f32_e32 v88, v128, v130
	v_add_f32_e32 v89, v129, v131
	v_exp_f32_e32 v136, v120
	v_exp_f32_e32 v137, v121
	v_exp_f32_e32 v138, v122
	v_mfma_f32_32x32x16_bf16 a[96:111], v[80:83], v[84:87], a[96:111]
	v_add_f32_e32 v84, v88, v132
	v_add_f32_e32 v85, v89, v133
	v_add_f32_e32 v84, v84, v134
	v_exp_f32_e32 v139, v123
	v_exp_f32_e32 v144, v96
	v_mfma_f32_32x32x16_bf16 a[112:127], v[80:83], v[140:143], a[112:127]
	v_add_f32_e32 v80, v85, v135
	v_add_f32_e32 v81, v84, v136
	v_exp_f32_e32 v140, v124
	v_exp_f32_e32 v141, v125
	v_add_f32_e32 v80, v80, v137
	v_mfma_f32_32x32x16_bf16 a[0:15], v[76:79], v[228:231], a[0:15]
	v_add_f32_e32 v81, v81, v138
	v_add_f32_e32 v80, v80, v139
	v_exp_f32_e32 v142, v126
	v_exp_f32_e32 v143, v127
	v_exp_f32_e32 v145, v97
	v_mfma_f32_32x32x16_bf16 a[16:31], v[76:79], v[160:163], a[16:31]
	v_add_f32_e32 v76, v81, v140
	v_add_f32_e32 v77, v80, v141
	v_exp_f32_e32 v146, v98
	v_add_f32_e32 v236, v76, v142
	v_add_f32_e32 v235, v77, v143
	v_exp_f32_e32 v147, v99
	v_mfma_f32_32x32x16_bf16 a[32:47], v[72:75], v[228:231], a[32:47]
	v_exp_f32_e32 v148, v100
	v_exp_f32_e32 v149, v101
	v_exp_f32_e32 v150, v102
	v_exp_f32_e32 v151, v103
	v_mfma_f32_32x32x16_bf16 a[48:63], v[72:75], v[160:163], a[48:63]
	v_add_f32_e32 v73, v144, v146
	v_add_f32_e32 v72, v145, v147
	v_add_f32_e32 v73, v73, v148
	v_add_f32_e32 v72, v72, v149
	v_exp_f32_e32 v152, v104
	v_exp_f32_e32 v153, v105
	v_mfma_f32_32x32x16_bf16 a[64:79], v[68:71], v[228:231], a[64:79]
	v_exp_f32_e32 v154, v106
	v_exp_f32_e32 v155, v107
	v_exp_f32_e32 v156, v108
	v_exp_f32_e32 v157, v109
	v_mfma_f32_32x32x16_bf16 a[80:95], v[68:71], v[160:163], a[80:95]
	v_add_f32_e32 v68, v73, v150
	v_add_f32_e32 v69, v72, v151
	v_add_f32_e32 v68, v68, v152
	v_add_f32_e32 v69, v69, v153
	v_add_f32_e32 v68, v68, v154
	v_exp_f32_e32 v158, v110
	v_mfma_f32_32x32x16_bf16 a[96:111], v[64:67], v[228:231], a[96:111]
	v_exp_f32_e32 v159, v111
	v_mfma_f32_32x32x16_bf16 a[112:127], v[64:67], v[160:163], a[112:127]
	v_add_f32_e32 v64, v69, v155
	v_add_f32_e32 v65, v68, v156
	s_andn2_b64 vcc, exec, s[0:1]
	v_add_f32_e32 v64, v64, v157
	v_add_f32_e32 v237, v65, v158
	s_nop 0
	v_add_f32_e32 v238, v64, v159
	s_cbranch_vccz .LBB0_25
